# down-projection epilogue hand-written: eight gate loads in flight with counted waits (was one load + vmcnt(0) per row group)
# speedup vs baseline: 1.0205x; 1.0019x over previous
; __device__ __forceinline__ unsigned cvt_pk_bf16(float lo, float hi) { unsigned r; asm volatile("v_cvt_pk_bf16_f32 %0, %1, %2" : "=v"(r) : "v"(lo), "v"(hi)); return r; }
;     DI void operator()(const pg8::f32x4 (&acc)[2][2][4][2], const pg8::Unit& u, int wr, int wc, int fr, int fq) const {
;         const int row0 = u.pm * 256 + wr * 64 + fr, col0 = (u.pn & 3) * 256 + wc * 32 + 8 * fq;
; #pragma unroll
;         for (int ai = 0; ai < 2; ++ai)
; #pragma unroll
;             for (int m = 0; m < 4; ++m) { const int row = row0 + ai * 128 + m * 16; const float g = gate[row] * (1.f / (F8_ASC * F8_WSC)); bf16* p = ys + (size_t)row * DM + col0;
; #pragma unroll
;                 for (int bj = 0; bj < 2; ++bj) { const pg8::f32x4 v0 = acc[ai][bj][m][0] * g, v1 = acc[ai][bj][m][1] * g; pg8::u32x4 w;
;                     w.x = pg8::cvt_pk_bf16(v0[0], v0[1]); w.y = pg8::cvt_pk_bf16(v0[2], v0[3]); w.z = pg8::cvt_pk_bf16(v1[0], v1[1]); w.w = pg8::cvt_pk_bf16(v1[2], v1[3]);
;                     *(pg8::u32x4*)(p + bj * 128) = w; } }
;     }
.LBB0_1465:
	v_lshl_add_u32 v252, s67, 8, v171
	s_lshl_b32 s70, s68, 8
	s_and_b32 s70, s70, 0x300
	v_or_b32_e32 v253, s70, v173
	v_lshlrev_b32_e32 v253, 1, v253
	v_lshl_add_u32 v253, v252, 11, v253
	v_lshlrev_b32_e32 v252, 2, v252
	global_load_dword v2, v252, s[18:19]
	global_load_dword v3, v252, s[18:19] offset:64
	global_load_dword v4, v252, s[18:19] offset:128
	global_load_dword v5, v252, s[18:19] offset:192
	global_load_dword v6, v252, s[18:19] offset:512
	global_load_dword v7, v252, s[18:19] offset:576
	global_load_dword v8, v252, s[18:19] offset:640
	global_load_dword v9, v252, s[18:19] offset:704
	s_waitcnt vmcnt(7)
	v_mul_f32_e32 v254, 0x3a800000, v2
	v_pk_mul_f32 v[122:123], v[122:123], v[254:255] op_sel_hi:[1,0]
	v_pk_mul_f32 v[124:125], v[124:125], v[254:255] op_sel_hi:[1,0]
	v_pk_mul_f32 v[126:127], v[126:127], v[254:255] op_sel_hi:[1,0]
	v_pk_mul_f32 v[128:129], v[128:129], v[254:255] op_sel_hi:[1,0]
	v_pk_mul_f32 v[130:131], v[130:131], v[254:255] op_sel_hi:[1,0]
	v_pk_mul_f32 v[132:133], v[132:133], v[254:255] op_sel_hi:[1,0]
	v_pk_mul_f32 v[134:135], v[134:135], v[254:255] op_sel_hi:[1,0]
	v_pk_mul_f32 v[136:137], v[136:137], v[254:255] op_sel_hi:[1,0]
	v_cvt_pk_bf16_f32 v122, v122, v123
	v_cvt_pk_bf16_f32 v123, v124, v125
	v_cvt_pk_bf16_f32 v124, v126, v127
	v_cvt_pk_bf16_f32 v125, v128, v129
	global_store_dwordx4 v253, v[122:125], s[16:17]
	v_cvt_pk_bf16_f32 v130, v130, v131
	v_cvt_pk_bf16_f32 v131, v132, v133
	v_cvt_pk_bf16_f32 v132, v134, v135
	v_cvt_pk_bf16_f32 v133, v136, v137
	global_store_dwordx4 v253, v[130:133], s[16:17] offset:256
	v_add_u32_e32 v253, 0x8000, v253
	s_waitcnt vmcnt(8)
	v_mul_f32_e32 v254, 0x3a800000, v3
	v_pk_mul_f32 v[106:107], v[106:107], v[254:255] op_sel_hi:[1,0]
	v_pk_mul_f32 v[108:109], v[108:109], v[254:255] op_sel_hi:[1,0]
	v_pk_mul_f32 v[110:111], v[110:111], v[254:255] op_sel_hi:[1,0]
	v_pk_mul_f32 v[112:113], v[112:113], v[254:255] op_sel_hi:[1,0]
	v_pk_mul_f32 v[114:115], v[114:115], v[254:255] op_sel_hi:[1,0]
	v_pk_mul_f32 v[116:117], v[116:117], v[254:255] op_sel_hi:[1,0]
	v_pk_mul_f32 v[118:119], v[118:119], v[254:255] op_sel_hi:[1,0]
	v_pk_mul_f32 v[120:121], v[120:121], v[254:255] op_sel_hi:[1,0]
	v_cvt_pk_bf16_f32 v106, v106, v107
	v_cvt_pk_bf16_f32 v107, v108, v109
	v_cvt_pk_bf16_f32 v108, v110, v111
	v_cvt_pk_bf16_f32 v109, v112, v113
	global_store_dwordx4 v253, v[106:109], s[16:17]
	v_cvt_pk_bf16_f32 v114, v114, v115
	v_cvt_pk_bf16_f32 v115, v116, v117
	v_cvt_pk_bf16_f32 v116, v118, v119
	v_cvt_pk_bf16_f32 v117, v120, v121
	global_store_dwordx4 v253, v[114:117], s[16:17] offset:256
	v_add_u32_e32 v253, 0x8000, v253
	s_waitcnt vmcnt(9)
	v_mul_f32_e32 v254, 0x3a800000, v4
	v_pk_mul_f32 v[90:91], v[90:91], v[254:255] op_sel_hi:[1,0]
	v_pk_mul_f32 v[92:93], v[92:93], v[254:255] op_sel_hi:[1,0]
	v_pk_mul_f32 v[94:95], v[94:95], v[254:255] op_sel_hi:[1,0]
	v_pk_mul_f32 v[96:97], v[96:97], v[254:255] op_sel_hi:[1,0]
	v_pk_mul_f32 v[98:99], v[98:99], v[254:255] op_sel_hi:[1,0]
	v_pk_mul_f32 v[100:101], v[100:101], v[254:255] op_sel_hi:[1,0]
	v_pk_mul_f32 v[102:103], v[102:103], v[254:255] op_sel_hi:[1,0]
	v_pk_mul_f32 v[104:105], v[104:105], v[254:255] op_sel_hi:[1,0]
	v_cvt_pk_bf16_f32 v90, v90, v91
	v_cvt_pk_bf16_f32 v91, v92, v93
	v_cvt_pk_bf16_f32 v92, v94, v95
	v_cvt_pk_bf16_f32 v93, v96, v97
	global_store_dwordx4 v253, v[90:93], s[16:17]
	v_cvt_pk_bf16_f32 v98, v98, v99
	v_cvt_pk_bf16_f32 v99, v100, v101
	v_cvt_pk_bf16_f32 v100, v102, v103
	v_cvt_pk_bf16_f32 v101, v104, v105
	global_store_dwordx4 v253, v[98:101], s[16:17] offset:256
	v_add_u32_e32 v253, 0x8000, v253
	s_waitcnt vmcnt(10)
	v_mul_f32_e32 v254, 0x3a800000, v5
	v_pk_mul_f32 v[82:83], v[82:83], v[254:255] op_sel_hi:[1,0]
	v_pk_mul_f32 v[84:85], v[84:85], v[254:255] op_sel_hi:[1,0]
	v_pk_mul_f32 v[86:87], v[86:87], v[254:255] op_sel_hi:[1,0]
	v_pk_mul_f32 v[88:89], v[88:89], v[254:255] op_sel_hi:[1,0]
	v_pk_mul_f32 v[74:75], v[74:75], v[254:255] op_sel_hi:[1,0]
	v_pk_mul_f32 v[76:77], v[76:77], v[254:255] op_sel_hi:[1,0]
	v_pk_mul_f32 v[78:79], v[78:79], v[254:255] op_sel_hi:[1,0]
	v_pk_mul_f32 v[80:81], v[80:81], v[254:255] op_sel_hi:[1,0]
	v_cvt_pk_bf16_f32 v82, v82, v83
	v_cvt_pk_bf16_f32 v83, v84, v85
	v_cvt_pk_bf16_f32 v84, v86, v87
	v_cvt_pk_bf16_f32 v85, v88, v89
	global_store_dwordx4 v253, v[82:85], s[16:17]
	v_cvt_pk_bf16_f32 v74, v74, v75
	v_cvt_pk_bf16_f32 v75, v76, v77
	v_cvt_pk_bf16_f32 v76, v78, v79
	v_cvt_pk_bf16_f32 v77, v80, v81
	global_store_dwordx4 v253, v[74:77], s[16:17] offset:256
	v_add_u32_e32 v253, 0x28000, v253
	s_waitcnt vmcnt(11)
	v_mul_f32_e32 v254, 0x3a800000, v6
	v_pk_mul_f32 v[66:67], v[66:67], v[254:255] op_sel_hi:[1,0]
	v_pk_mul_f32 v[68:69], v[68:69], v[254:255] op_sel_hi:[1,0]
	v_pk_mul_f32 v[70:71], v[70:71], v[254:255] op_sel_hi:[1,0]
	v_pk_mul_f32 v[72:73], v[72:73], v[254:255] op_sel_hi:[1,0]
	v_pk_mul_f32 v[58:59], v[58:59], v[254:255] op_sel_hi:[1,0]
	v_pk_mul_f32 v[60:61], v[60:61], v[254:255] op_sel_hi:[1,0]
	v_pk_mul_f32 v[62:63], v[62:63], v[254:255] op_sel_hi:[1,0]
	v_pk_mul_f32 v[64:65], v[64:65], v[254:255] op_sel_hi:[1,0]
	v_cvt_pk_bf16_f32 v66, v66, v67
	v_cvt_pk_bf16_f32 v67, v68, v69
	v_cvt_pk_bf16_f32 v68, v70, v71
	v_cvt_pk_bf16_f32 v69, v72, v73
	global_store_dwordx4 v253, v[66:69], s[16:17]
	v_cvt_pk_bf16_f32 v58, v58, v59
	v_cvt_pk_bf16_f32 v59, v60, v61
	v_cvt_pk_bf16_f32 v60, v62, v63
	v_cvt_pk_bf16_f32 v61, v64, v65
	global_store_dwordx4 v253, v[58:61], s[16:17] offset:256
	v_add_u32_e32 v253, 0x8000, v253
	s_waitcnt vmcnt(12)
; __device__ __forceinline__ unsigned cvt_pk_bf16(float lo, float hi) { unsigned r; asm volatile("v_cvt_pk_bf16_f32 %0, %1, %2" : "=v"(r) : "v"(lo), "v"(hi)); return r; }
; #define PG8_BAR __builtin_amdgcn_s_barrier()
; template <class Epi, class Sched, bool ALIGN_EPI = false, bool SP2 = false, bool F8 = false>
; __device__ __forceinline__ void gemm_phase(PG8_LAS unsigned char* lds, const Gemm g, const Sched& S, const Epi& E) {
;     ...
; #pragma unroll
;         for (int a = 0; a < 2; ++a)
; #pragma unroll
;             for (int b = 0; b < 2; ++b)
; #pragma unroll
;                 for (int m = 0; m < 4; ++m)
; #pragma unroll
;                     for (int n = 0; n < 2; ++n) { acc[a][b][m][n] = (f32x4){0.f, 0.f, 0.f, 0.f}; if constexpr (F8) asm volatile("" : "+v"(acc[a][b][m][n])); }
;         cur = nxt; cA = nA; cB = nB; ++ui;
;         if constexpr (ALIGN_EPI) { if (wr == 1) PG8_BAR; }
;     DI void operator()(const pg8::f32x4 (&acc)[2][2][4][2], const pg8::Unit& u, int wr, int wc, int fr, int fq) const {
;     ...
;             for (int m = 0; m < 4; ++m) { const int row = row0 + ai * 128 + m * 16; const float g = gate[row] * (1.f / (F8_ASC * F8_WSC)); bf16* p = ys + (size_t)row * DM + col0;
; #pragma unroll
;                 for (int bj = 0; bj < 2; ++bj) { const pg8::f32x4 v0 = acc[ai][bj][m][0] * g, v1 = acc[ai][bj][m][1] * g; pg8::u32x4 w;
;                     w.x = pg8::cvt_pk_bf16(v0[0], v0[1]); w.y = pg8::cvt_pk_bf16(v0[2], v0[3]); w.z = pg8::cvt_pk_bf16(v1[0], v1[1]); w.w = pg8::cvt_pk_bf16(v1[2], v1[3]);
;                     *(pg8::u32x4*)(p + bj * 128) = w; } }
;     }
	v_mul_f32_e32 v254, 0x3a800000, v7
	v_pk_mul_f32 v[50:51], v[50:51], v[254:255] op_sel_hi:[1,0]
	v_pk_mul_f32 v[52:53], v[52:53], v[254:255] op_sel_hi:[1,0]
	v_pk_mul_f32 v[54:55], v[54:55], v[254:255] op_sel_hi:[1,0]
	v_pk_mul_f32 v[56:57], v[56:57], v[254:255] op_sel_hi:[1,0]
	v_pk_mul_f32 v[42:43], v[42:43], v[254:255] op_sel_hi:[1,0]
	v_pk_mul_f32 v[44:45], v[44:45], v[254:255] op_sel_hi:[1,0]
	v_pk_mul_f32 v[46:47], v[46:47], v[254:255] op_sel_hi:[1,0]
	v_pk_mul_f32 v[48:49], v[48:49], v[254:255] op_sel_hi:[1,0]
	v_cvt_pk_bf16_f32 v50, v50, v51
	v_cvt_pk_bf16_f32 v51, v52, v53
	v_cvt_pk_bf16_f32 v52, v54, v55
	v_cvt_pk_bf16_f32 v53, v56, v57
	global_store_dwordx4 v253, v[50:53], s[16:17]
	v_cvt_pk_bf16_f32 v42, v42, v43
	v_cvt_pk_bf16_f32 v43, v44, v45
	v_cvt_pk_bf16_f32 v44, v46, v47
	v_cvt_pk_bf16_f32 v45, v48, v49
	global_store_dwordx4 v253, v[42:45], s[16:17] offset:256
	v_add_u32_e32 v253, 0x8000, v253
	s_waitcnt vmcnt(13)
	v_mul_f32_e32 v254, 0x3a800000, v8
	v_pk_mul_f32 v[34:35], v[34:35], v[254:255] op_sel_hi:[1,0]
	v_pk_mul_f32 v[36:37], v[36:37], v[254:255] op_sel_hi:[1,0]
	v_pk_mul_f32 v[38:39], v[38:39], v[254:255] op_sel_hi:[1,0]
	v_pk_mul_f32 v[40:41], v[40:41], v[254:255] op_sel_hi:[1,0]
	v_pk_mul_f32 v[26:27], v[26:27], v[254:255] op_sel_hi:[1,0]
	v_pk_mul_f32 v[28:29], v[28:29], v[254:255] op_sel_hi:[1,0]
	v_pk_mul_f32 v[30:31], v[30:31], v[254:255] op_sel_hi:[1,0]
	v_pk_mul_f32 v[32:33], v[32:33], v[254:255] op_sel_hi:[1,0]
	v_cvt_pk_bf16_f32 v34, v34, v35
	v_cvt_pk_bf16_f32 v35, v36, v37
	v_cvt_pk_bf16_f32 v36, v38, v39
	v_cvt_pk_bf16_f32 v37, v40, v41
	global_store_dwordx4 v253, v[34:37], s[16:17]
	v_cvt_pk_bf16_f32 v26, v26, v27
	v_cvt_pk_bf16_f32 v27, v28, v29
	v_cvt_pk_bf16_f32 v28, v30, v31
	v_cvt_pk_bf16_f32 v29, v32, v33
	global_store_dwordx4 v253, v[26:29], s[16:17] offset:256
	v_add_u32_e32 v253, 0x8000, v253
	s_waitcnt vmcnt(14)
	v_mul_f32_e32 v254, 0x3a800000, v9
	v_pk_mul_f32 v[14:15], v[14:15], v[254:255] op_sel_hi:[1,0]
	v_pk_mul_f32 v[16:17], v[16:17], v[254:255] op_sel_hi:[1,0]
	v_pk_mul_f32 v[18:19], v[18:19], v[254:255] op_sel_hi:[1,0]
	v_pk_mul_f32 v[20:21], v[20:21], v[254:255] op_sel_hi:[1,0]
	v_pk_mul_f32 v[22:23], v[22:23], v[254:255] op_sel_hi:[1,0]
	v_pk_mul_f32 v[24:25], v[24:25], v[254:255] op_sel_hi:[1,0]
	v_pk_mul_f32 v[10:11], v[10:11], v[254:255] op_sel_hi:[1,0]
	v_pk_mul_f32 v[12:13], v[12:13], v[254:255] op_sel_hi:[1,0]
	v_cvt_pk_bf16_f32 v14, v14, v15
	v_cvt_pk_bf16_f32 v15, v16, v17
	v_cvt_pk_bf16_f32 v16, v18, v19
	v_cvt_pk_bf16_f32 v17, v20, v21
	global_store_dwordx4 v253, v[14:17], s[16:17]
	v_cvt_pk_bf16_f32 v22, v22, v23
	v_cvt_pk_bf16_f32 v23, v24, v25
	v_cvt_pk_bf16_f32 v24, v10, v11
	v_cvt_pk_bf16_f32 v25, v12, v13
	global_store_dwordx4 v253, v[22:25], s[16:17] offset:256
	s_mov_b64 s[10:11], -1
	s_and_b64 vcc, exec, s[4:5]
	s_cbranch_vccnz .LBB0_1453
	s_mov_b32 s10, s8
	s_mov_b32 s11, s8
	s_mov_b32 s9, s8
	v_mov_b64_e32 v[12:13], s[10:11]
	v_mov_b64_e32 v[124:125], s[10:11]
	v_mov_b64_e32 v[128:129], s[10:11]
	v_mov_b64_e32 v[108:109], s[10:11]
	v_mov_b64_e32 v[112:113], s[10:11]
	v_mov_b64_e32 v[92:93], s[10:11]
	v_mov_b64_e32 v[96:97], s[10:11]
	v_mov_b64_e32 v[84:85], s[10:11]
	v_mov_b64_e32 v[88:89], s[10:11]
	v_mov_b64_e32 v[132:133], s[10:11]
	v_mov_b64_e32 v[136:137], s[10:11]
	v_mov_b64_e32 v[116:117], s[10:11]
	v_mov_b64_e32 v[120:121], s[10:11]
	v_mov_b64_e32 v[100:101], s[10:11]
	v_mov_b64_e32 v[104:105], s[10:11]
	v_mov_b64_e32 v[76:77], s[10:11]
	v_mov_b64_e32 v[80:81], s[10:11]
	v_mov_b64_e32 v[68:69], s[10:11]
	v_mov_b64_e32 v[72:73], s[10:11]
	v_mov_b64_e32 v[52:53], s[10:11]
	v_mov_b64_e32 v[56:57], s[10:11]
	v_mov_b64_e32 v[36:37], s[10:11]
	v_mov_b64_e32 v[40:41], s[10:11]
	v_mov_b64_e32 v[16:17], s[10:11]
	v_mov_b64_e32 v[20:21], s[10:11]
	v_mov_b64_e32 v[60:61], s[10:11]
	v_mov_b64_e32 v[64:65], s[10:11]
	v_mov_b64_e32 v[44:45], s[10:11]
	v_mov_b64_e32 v[48:49], s[10:11]
	v_mov_b64_e32 v[28:29], s[10:11]
	v_mov_b64_e32 v[32:33], s[10:11]
	v_mov_b64_e32 v[24:25], s[10:11]
	v_mov_b64_e32 v[10:11], s[8:9]
	v_mov_b64_e32 v[122:123], s[8:9]
	v_mov_b64_e32 v[126:127], s[8:9]
	v_mov_b64_e32 v[106:107], s[8:9]
	v_mov_b64_e32 v[110:111], s[8:9]
	v_mov_b64_e32 v[90:91], s[8:9]
	v_mov_b64_e32 v[94:95], s[8:9]
	v_mov_b64_e32 v[82:83], s[8:9]
	v_mov_b64_e32 v[86:87], s[8:9]
	v_mov_b64_e32 v[130:131], s[8:9]
	v_mov_b64_e32 v[134:135], s[8:9]
	v_mov_b64_e32 v[114:115], s[8:9]
	v_mov_b64_e32 v[118:119], s[8:9]
	v_mov_b64_e32 v[98:99], s[8:9]
	v_mov_b64_e32 v[102:103], s[8:9]
	v_mov_b64_e32 v[74:75], s[8:9]
	v_mov_b64_e32 v[78:79], s[8:9]
	v_mov_b64_e32 v[66:67], s[8:9]
	v_mov_b64_e32 v[70:71], s[8:9]
	v_mov_b64_e32 v[50:51], s[8:9]
	v_mov_b64_e32 v[54:55], s[8:9]
	v_mov_b64_e32 v[34:35], s[8:9]
	v_mov_b64_e32 v[38:39], s[8:9]
	v_mov_b64_e32 v[14:15], s[8:9]
	v_mov_b64_e32 v[18:19], s[8:9]
	v_mov_b64_e32 v[58:59], s[8:9]
	v_mov_b64_e32 v[62:63], s[8:9]
	v_mov_b64_e32 v[42:43], s[8:9]
	v_mov_b64_e32 v[46:47], s[8:9]
	v_mov_b64_e32 v[26:27], s[8:9]
	v_mov_b64_e32 v[30:31], s[8:9]
	v_mov_b64_e32 v[22:23], s[8:9]
	s_andn2_b64 vcc, exec, s[14:15]
	s_cbranch_vccnz .LBB0_1452
	s_barrier
	s_branch .LBB0_1452

; __device__ __forceinline__ unsigned cvt_pk_bf16(float lo, float hi) { unsigned r; asm volatile("v_cvt_pk_bf16_f32 %0, %1, %2" : "=v"(r) : "v"(lo), "v"(hi)); return r; }
;     DI void operator()(const pg8::f32x4 (&acc)[2][2][4][2], const pg8::Unit& u, int wr, int wc, int fr, int fq) const {
;         const int row0 = u.pm * 256 + wr * 64 + fr, col0 = (u.pn & 3) * 256 + wc * 32 + 8 * fq;
; #pragma unroll
;         for (int ai = 0; ai < 2; ++ai)
; #pragma unroll
;             for (int m = 0; m < 4; ++m) { const int row = row0 + ai * 128 + m * 16; const float g = gate[row] * (1.f / (F8_ASC * F8_WSC)); bf16* p = ys + (size_t)row * DM + col0;
; #pragma unroll
;                 for (int bj = 0; bj < 2; ++bj) { const pg8::f32x4 v0 = acc[ai][bj][m][0] * g, v1 = acc[ai][bj][m][1] * g; pg8::u32x4 w;
;                     w.x = pg8::cvt_pk_bf16(v0[0], v0[1]); w.y = pg8::cvt_pk_bf16(v0[2], v0[3]); w.z = pg8::cvt_pk_bf16(v1[0], v1[1]); w.w = pg8::cvt_pk_bf16(v1[2], v1[3]);
;                     *(pg8::u32x4*)(p + bj * 128) = w; } }
;     }
.LBB0_2894:
	v_lshl_add_u32 v252, s67, 8, v147
	s_lshl_b32 s70, s66, 8
	s_and_b32 s70, s70, 0x300
	v_or_b32_e32 v253, s70, v171
	v_lshlrev_b32_e32 v253, 1, v253
	v_lshl_add_u32 v253, v252, 11, v253
	v_lshlrev_b32_e32 v252, 2, v252
	global_load_dword v2, v252, s[18:19]
	global_load_dword v3, v252, s[18:19] offset:64
	global_load_dword v4, v252, s[18:19] offset:128
	global_load_dword v5, v252, s[18:19] offset:192
	global_load_dword v6, v252, s[18:19] offset:512
	global_load_dword v7, v252, s[18:19] offset:576
	global_load_dword v8, v252, s[18:19] offset:640
	global_load_dword v9, v252, s[18:19] offset:704
	s_waitcnt vmcnt(7)
	v_mul_f32_e32 v254, 0x3a800000, v2
	v_pk_mul_f32 v[122:123], v[122:123], v[254:255] op_sel_hi:[1,0]
	v_pk_mul_f32 v[124:125], v[124:125], v[254:255] op_sel_hi:[1,0]
	v_pk_mul_f32 v[126:127], v[126:127], v[254:255] op_sel_hi:[1,0]
	v_pk_mul_f32 v[128:129], v[128:129], v[254:255] op_sel_hi:[1,0]
	v_pk_mul_f32 v[130:131], v[130:131], v[254:255] op_sel_hi:[1,0]
	v_pk_mul_f32 v[132:133], v[132:133], v[254:255] op_sel_hi:[1,0]
	v_pk_mul_f32 v[134:135], v[134:135], v[254:255] op_sel_hi:[1,0]
	v_pk_mul_f32 v[136:137], v[136:137], v[254:255] op_sel_hi:[1,0]
	v_cvt_pk_bf16_f32 v122, v122, v123
	v_cvt_pk_bf16_f32 v123, v124, v125
	v_cvt_pk_bf16_f32 v124, v126, v127
	v_cvt_pk_bf16_f32 v125, v128, v129
	global_store_dwordx4 v253, v[122:125], s[16:17]
	v_cvt_pk_bf16_f32 v130, v130, v131
	v_cvt_pk_bf16_f32 v131, v132, v133
	v_cvt_pk_bf16_f32 v132, v134, v135
	v_cvt_pk_bf16_f32 v133, v136, v137
	global_store_dwordx4 v253, v[130:133], s[16:17] offset:256
	v_add_u32_e32 v253, 0x8000, v253
	s_waitcnt vmcnt(8)
	v_mul_f32_e32 v254, 0x3a800000, v3
	v_pk_mul_f32 v[106:107], v[106:107], v[254:255] op_sel_hi:[1,0]
	v_pk_mul_f32 v[108:109], v[108:109], v[254:255] op_sel_hi:[1,0]
	v_pk_mul_f32 v[110:111], v[110:111], v[254:255] op_sel_hi:[1,0]
	v_pk_mul_f32 v[112:113], v[112:113], v[254:255] op_sel_hi:[1,0]
	v_pk_mul_f32 v[114:115], v[114:115], v[254:255] op_sel_hi:[1,0]
	v_pk_mul_f32 v[116:117], v[116:117], v[254:255] op_sel_hi:[1,0]
	v_pk_mul_f32 v[118:119], v[118:119], v[254:255] op_sel_hi:[1,0]
	v_pk_mul_f32 v[120:121], v[120:121], v[254:255] op_sel_hi:[1,0]
	v_cvt_pk_bf16_f32 v106, v106, v107
	v_cvt_pk_bf16_f32 v107, v108, v109
	v_cvt_pk_bf16_f32 v108, v110, v111
	v_cvt_pk_bf16_f32 v109, v112, v113
	global_store_dwordx4 v253, v[106:109], s[16:17]
	v_cvt_pk_bf16_f32 v114, v114, v115
	v_cvt_pk_bf16_f32 v115, v116, v117
	v_cvt_pk_bf16_f32 v116, v118, v119
	v_cvt_pk_bf16_f32 v117, v120, v121
	global_store_dwordx4 v253, v[114:117], s[16:17] offset:256
	v_add_u32_e32 v253, 0x8000, v253
	s_waitcnt vmcnt(9)
	v_mul_f32_e32 v254, 0x3a800000, v4
	v_pk_mul_f32 v[90:91], v[90:91], v[254:255] op_sel_hi:[1,0]
	v_pk_mul_f32 v[92:93], v[92:93], v[254:255] op_sel_hi:[1,0]
	v_pk_mul_f32 v[94:95], v[94:95], v[254:255] op_sel_hi:[1,0]
	v_pk_mul_f32 v[96:97], v[96:97], v[254:255] op_sel_hi:[1,0]
	v_pk_mul_f32 v[98:99], v[98:99], v[254:255] op_sel_hi:[1,0]
	v_pk_mul_f32 v[100:101], v[100:101], v[254:255] op_sel_hi:[1,0]
	v_pk_mul_f32 v[102:103], v[102:103], v[254:255] op_sel_hi:[1,0]
	v_pk_mul_f32 v[104:105], v[104:105], v[254:255] op_sel_hi:[1,0]
	v_cvt_pk_bf16_f32 v90, v90, v91
	v_cvt_pk_bf16_f32 v91, v92, v93
	v_cvt_pk_bf16_f32 v92, v94, v95
	v_cvt_pk_bf16_f32 v93, v96, v97
	global_store_dwordx4 v253, v[90:93], s[16:17]
	v_cvt_pk_bf16_f32 v98, v98, v99
	v_cvt_pk_bf16_f32 v99, v100, v101
	v_cvt_pk_bf16_f32 v100, v102, v103
	v_cvt_pk_bf16_f32 v101, v104, v105
	global_store_dwordx4 v253, v[98:101], s[16:17] offset:256
	v_add_u32_e32 v253, 0x8000, v253
	s_waitcnt vmcnt(10)
	v_mul_f32_e32 v254, 0x3a800000, v5
	v_pk_mul_f32 v[74:75], v[74:75], v[254:255] op_sel_hi:[1,0]
	v_pk_mul_f32 v[76:77], v[76:77], v[254:255] op_sel_hi:[1,0]
	v_pk_mul_f32 v[78:79], v[78:79], v[254:255] op_sel_hi:[1,0]
	v_pk_mul_f32 v[80:81], v[80:81], v[254:255] op_sel_hi:[1,0]
	v_pk_mul_f32 v[82:83], v[82:83], v[254:255] op_sel_hi:[1,0]
	v_pk_mul_f32 v[84:85], v[84:85], v[254:255] op_sel_hi:[1,0]
	v_pk_mul_f32 v[86:87], v[86:87], v[254:255] op_sel_hi:[1,0]
	v_pk_mul_f32 v[88:89], v[88:89], v[254:255] op_sel_hi:[1,0]
	v_cvt_pk_bf16_f32 v74, v74, v75
	v_cvt_pk_bf16_f32 v75, v76, v77
	v_cvt_pk_bf16_f32 v76, v78, v79
	v_cvt_pk_bf16_f32 v77, v80, v81
	global_store_dwordx4 v253, v[74:77], s[16:17]
	v_cvt_pk_bf16_f32 v82, v82, v83
	v_cvt_pk_bf16_f32 v83, v84, v85
	v_cvt_pk_bf16_f32 v84, v86, v87
	v_cvt_pk_bf16_f32 v85, v88, v89
	global_store_dwordx4 v253, v[82:85], s[16:17] offset:256
	v_add_u32_e32 v253, 0x28000, v253
	s_waitcnt vmcnt(11)
	v_mul_f32_e32 v254, 0x3a800000, v6
	v_pk_mul_f32 v[58:59], v[58:59], v[254:255] op_sel_hi:[1,0]
	v_pk_mul_f32 v[60:61], v[60:61], v[254:255] op_sel_hi:[1,0]
	v_pk_mul_f32 v[62:63], v[62:63], v[254:255] op_sel_hi:[1,0]
	v_pk_mul_f32 v[64:65], v[64:65], v[254:255] op_sel_hi:[1,0]
	v_pk_mul_f32 v[66:67], v[66:67], v[254:255] op_sel_hi:[1,0]
	v_pk_mul_f32 v[68:69], v[68:69], v[254:255] op_sel_hi:[1,0]
	v_pk_mul_f32 v[70:71], v[70:71], v[254:255] op_sel_hi:[1,0]
	v_pk_mul_f32 v[72:73], v[72:73], v[254:255] op_sel_hi:[1,0]
	v_cvt_pk_bf16_f32 v58, v58, v59
	v_cvt_pk_bf16_f32 v59, v60, v61
	v_cvt_pk_bf16_f32 v60, v62, v63
	v_cvt_pk_bf16_f32 v61, v64, v65
	global_store_dwordx4 v253, v[58:61], s[16:17]
	v_cvt_pk_bf16_f32 v66, v66, v67
	v_cvt_pk_bf16_f32 v67, v68, v69
	v_cvt_pk_bf16_f32 v68, v70, v71
	v_cvt_pk_bf16_f32 v69, v72, v73
	global_store_dwordx4 v253, v[66:69], s[16:17] offset:256
	v_add_u32_e32 v253, 0x8000, v253
	s_waitcnt vmcnt(12)
; __device__ __forceinline__ unsigned cvt_pk_bf16(float lo, float hi) { unsigned r; asm volatile("v_cvt_pk_bf16_f32 %0, %1, %2" : "=v"(r) : "v"(lo), "v"(hi)); return r; }
; #define PG8_BAR __builtin_amdgcn_s_barrier()
; template <class Epi, class Sched, bool ALIGN_EPI = false, bool SP2 = false, bool F8 = false>
; __device__ __forceinline__ void gemm_phase(PG8_LAS unsigned char* lds, const Gemm g, const Sched& S, const Epi& E) {
;     ...
; #pragma unroll
;         for (int a = 0; a < 2; ++a)
; #pragma unroll
;             for (int b = 0; b < 2; ++b)
; #pragma unroll
;                 for (int m = 0; m < 4; ++m)
; #pragma unroll
;                     for (int n = 0; n < 2; ++n) { acc[a][b][m][n] = (f32x4){0.f, 0.f, 0.f, 0.f}; if constexpr (F8) asm volatile("" : "+v"(acc[a][b][m][n])); }
;         cur = nxt; cA = nA; cB = nB; ++ui;
;         if constexpr (ALIGN_EPI) { if (wr == 1) PG8_BAR; }
;     DI void operator()(const pg8::f32x4 (&acc)[2][2][4][2], const pg8::Unit& u, int wr, int wc, int fr, int fq) const {
;     ...
;             for (int m = 0; m < 4; ++m) { const int row = row0 + ai * 128 + m * 16; const float g = gate[row] * (1.f / (F8_ASC * F8_WSC)); bf16* p = ys + (size_t)row * DM + col0;
; #pragma unroll
;                 for (int bj = 0; bj < 2; ++bj) { const pg8::f32x4 v0 = acc[ai][bj][m][0] * g, v1 = acc[ai][bj][m][1] * g; pg8::u32x4 w;
;                     w.x = pg8::cvt_pk_bf16(v0[0], v0[1]); w.y = pg8::cvt_pk_bf16(v0[2], v0[3]); w.z = pg8::cvt_pk_bf16(v1[0], v1[1]); w.w = pg8::cvt_pk_bf16(v1[2], v1[3]);
;                     *(pg8::u32x4*)(p + bj * 128) = w; } }
;     }
	v_mul_f32_e32 v254, 0x3a800000, v7
	v_pk_mul_f32 v[42:43], v[42:43], v[254:255] op_sel_hi:[1,0]
	v_pk_mul_f32 v[44:45], v[44:45], v[254:255] op_sel_hi:[1,0]
	v_pk_mul_f32 v[46:47], v[46:47], v[254:255] op_sel_hi:[1,0]
	v_pk_mul_f32 v[48:49], v[48:49], v[254:255] op_sel_hi:[1,0]
	v_pk_mul_f32 v[50:51], v[50:51], v[254:255] op_sel_hi:[1,0]
	v_pk_mul_f32 v[52:53], v[52:53], v[254:255] op_sel_hi:[1,0]
	v_pk_mul_f32 v[54:55], v[54:55], v[254:255] op_sel_hi:[1,0]
	v_pk_mul_f32 v[56:57], v[56:57], v[254:255] op_sel_hi:[1,0]
	v_cvt_pk_bf16_f32 v42, v42, v43
	v_cvt_pk_bf16_f32 v43, v44, v45
	v_cvt_pk_bf16_f32 v44, v46, v47
	v_cvt_pk_bf16_f32 v45, v48, v49
	global_store_dwordx4 v253, v[42:45], s[16:17]
	v_cvt_pk_bf16_f32 v50, v50, v51
	v_cvt_pk_bf16_f32 v51, v52, v53
	v_cvt_pk_bf16_f32 v52, v54, v55
	v_cvt_pk_bf16_f32 v53, v56, v57
	global_store_dwordx4 v253, v[50:53], s[16:17] offset:256
	v_add_u32_e32 v253, 0x8000, v253
	s_waitcnt vmcnt(13)
	v_mul_f32_e32 v254, 0x3a800000, v8
	v_pk_mul_f32 v[26:27], v[26:27], v[254:255] op_sel_hi:[1,0]
	v_pk_mul_f32 v[28:29], v[28:29], v[254:255] op_sel_hi:[1,0]
	v_pk_mul_f32 v[30:31], v[30:31], v[254:255] op_sel_hi:[1,0]
	v_pk_mul_f32 v[32:33], v[32:33], v[254:255] op_sel_hi:[1,0]
	v_pk_mul_f32 v[34:35], v[34:35], v[254:255] op_sel_hi:[1,0]
	v_pk_mul_f32 v[36:37], v[36:37], v[254:255] op_sel_hi:[1,0]
	v_pk_mul_f32 v[38:39], v[38:39], v[254:255] op_sel_hi:[1,0]
	v_pk_mul_f32 v[40:41], v[40:41], v[254:255] op_sel_hi:[1,0]
	v_cvt_pk_bf16_f32 v26, v26, v27
	v_cvt_pk_bf16_f32 v27, v28, v29
	v_cvt_pk_bf16_f32 v28, v30, v31
	v_cvt_pk_bf16_f32 v29, v32, v33
	global_store_dwordx4 v253, v[26:29], s[16:17]
	v_cvt_pk_bf16_f32 v34, v34, v35
	v_cvt_pk_bf16_f32 v35, v36, v37
	v_cvt_pk_bf16_f32 v36, v38, v39
	v_cvt_pk_bf16_f32 v37, v40, v41
	global_store_dwordx4 v253, v[34:37], s[16:17] offset:256
	v_add_u32_e32 v253, 0x8000, v253
	s_waitcnt vmcnt(14)
	v_mul_f32_e32 v254, 0x3a800000, v9
	v_pk_mul_f32 v[14:15], v[14:15], v[254:255] op_sel_hi:[1,0]
	v_pk_mul_f32 v[16:17], v[16:17], v[254:255] op_sel_hi:[1,0]
	v_pk_mul_f32 v[18:19], v[18:19], v[254:255] op_sel_hi:[1,0]
	v_pk_mul_f32 v[20:21], v[20:21], v[254:255] op_sel_hi:[1,0]
	v_pk_mul_f32 v[22:23], v[22:23], v[254:255] op_sel_hi:[1,0]
	v_pk_mul_f32 v[24:25], v[24:25], v[254:255] op_sel_hi:[1,0]
	v_pk_mul_f32 v[10:11], v[10:11], v[254:255] op_sel_hi:[1,0]
	v_pk_mul_f32 v[12:13], v[12:13], v[254:255] op_sel_hi:[1,0]
	v_cvt_pk_bf16_f32 v14, v14, v15
	v_cvt_pk_bf16_f32 v15, v16, v17
	v_cvt_pk_bf16_f32 v16, v18, v19
	v_cvt_pk_bf16_f32 v17, v20, v21
	global_store_dwordx4 v253, v[14:17], s[16:17]
	v_cvt_pk_bf16_f32 v22, v22, v23
	v_cvt_pk_bf16_f32 v23, v24, v25
	v_cvt_pk_bf16_f32 v24, v10, v11
	v_cvt_pk_bf16_f32 v25, v12, v13
	global_store_dwordx4 v253, v[22:25], s[16:17] offset:256
	s_and_b64 vcc, exec, s[0:1]
	s_mov_b64 s[0:1], -1
	s_cbranch_vccnz .LBB0_2882
	s_mov_b32 s6, s4
	s_mov_b32 s7, s4
	s_mov_b32 s5, s4
	v_mov_b64_e32 v[12:13], s[6:7]
	v_mov_b64_e32 v[124:125], s[6:7]
	v_mov_b64_e32 v[128:129], s[6:7]
	v_mov_b64_e32 v[108:109], s[6:7]
	v_mov_b64_e32 v[112:113], s[6:7]
	v_mov_b64_e32 v[92:93], s[6:7]
	v_mov_b64_e32 v[96:97], s[6:7]
	v_mov_b64_e32 v[76:77], s[6:7]
	v_mov_b64_e32 v[80:81], s[6:7]
	v_mov_b64_e32 v[132:133], s[6:7]
	v_mov_b64_e32 v[136:137], s[6:7]
	v_mov_b64_e32 v[116:117], s[6:7]
	v_mov_b64_e32 v[120:121], s[6:7]
	v_mov_b64_e32 v[100:101], s[6:7]
	v_mov_b64_e32 v[104:105], s[6:7]
	v_mov_b64_e32 v[84:85], s[6:7]
	v_mov_b64_e32 v[88:89], s[6:7]
	v_mov_b64_e32 v[60:61], s[6:7]
	v_mov_b64_e32 v[64:65], s[6:7]
	v_mov_b64_e32 v[44:45], s[6:7]
	v_mov_b64_e32 v[48:49], s[6:7]
	v_mov_b64_e32 v[28:29], s[6:7]
	v_mov_b64_e32 v[32:33], s[6:7]
	v_mov_b64_e32 v[16:17], s[6:7]
	v_mov_b64_e32 v[20:21], s[6:7]
	v_mov_b64_e32 v[68:69], s[6:7]
	v_mov_b64_e32 v[72:73], s[6:7]
	v_mov_b64_e32 v[52:53], s[6:7]
	v_mov_b64_e32 v[56:57], s[6:7]
	v_mov_b64_e32 v[36:37], s[6:7]
	v_mov_b64_e32 v[40:41], s[6:7]
	v_mov_b64_e32 v[24:25], s[6:7]
	v_mov_b64_e32 v[10:11], s[4:5]
	v_mov_b64_e32 v[122:123], s[4:5]
	v_mov_b64_e32 v[126:127], s[4:5]
	v_mov_b64_e32 v[106:107], s[4:5]
	v_mov_b64_e32 v[110:111], s[4:5]
	v_mov_b64_e32 v[90:91], s[4:5]
	v_mov_b64_e32 v[94:95], s[4:5]
	v_mov_b64_e32 v[74:75], s[4:5]
	v_mov_b64_e32 v[78:79], s[4:5]
	v_mov_b64_e32 v[130:131], s[4:5]
	v_mov_b64_e32 v[134:135], s[4:5]
	v_mov_b64_e32 v[114:115], s[4:5]
	v_mov_b64_e32 v[118:119], s[4:5]
	v_mov_b64_e32 v[98:99], s[4:5]
	v_mov_b64_e32 v[102:103], s[4:5]
	v_mov_b64_e32 v[82:83], s[4:5]
	v_mov_b64_e32 v[86:87], s[4:5]
	v_mov_b64_e32 v[58:59], s[4:5]
	v_mov_b64_e32 v[62:63], s[4:5]
	v_mov_b64_e32 v[42:43], s[4:5]
	v_mov_b64_e32 v[46:47], s[4:5]
	v_mov_b64_e32 v[26:27], s[4:5]
	v_mov_b64_e32 v[30:31], s[4:5]
	v_mov_b64_e32 v[14:15], s[4:5]
	v_mov_b64_e32 v[18:19], s[4:5]
	v_mov_b64_e32 v[66:67], s[4:5]
	v_mov_b64_e32 v[70:71], s[4:5]
	v_mov_b64_e32 v[50:51], s[4:5]
	v_mov_b64_e32 v[54:55], s[4:5]
	v_mov_b64_e32 v[34:35], s[4:5]
	v_mov_b64_e32 v[38:39], s[4:5]
	v_mov_b64_e32 v[22:23], s[4:5]
	s_andn2_b64 vcc, exec, s[14:15]
	s_cbranch_vccnz .LBB0_2881
	s_barrier
	s_branch .LBB0_2881
